# best + 32-level ~100ns per-CU start skew in P6/P7/P10/P11
# baseline (speedup 1.0000x reference)
;     __device__ __forceinline__ void init(int G_, int c_) { G = G_; c = c_; so.init(M, NPROJ, G_, c_); }
;     __device__ __forceinline__ bool next(int i, pg8::Unit& u) const { const int s = i >= R ? 1 : 0; const bool ok = so.next(i - s * R, u); u.sel = s; return ok && i < 2 * R; }
; #define PHASE_BASES() const KAS char* KA = (const KAS char*)__builtin_amdgcn_kernarg_segment_ptr(); asm volatile("" : "+s"(KA)); unsigned char* const ws = *(unsigned char* const KAS*)(KA + 8 * 27)
;     __host__ __device__ __forceinline__ bool next(int i, Unit& u) const {
;         const long L = (long)i * G + c; if (L >= nwg) return false;
;         int wgid = (int)L; { const int q = nwg / NXCD, r = nwg % NXCD, xcd = wgid % NXCD, off = wgid / NXCD; wgid = (xcd < r ? xcd * (q + 1) : r * (q + 1) + (xcd - r) * q) + off; }
;         const int nig = WGM * nN, gid = wgid / nig, fm = gid * WGM, gsz = (nM - fm) < WGM ? (nM - fm) : WGM;
;         u.pm = fm + ((wgid % nig) % gsz); u.pn = (wgid % nig) / gsz; return true;
; __global__ void __launch_bounds__(NWAVES * 64, 2) mk_fwd(Args args) {
;     ...
;     if (IN(6)) { PHASE_BASES();
;         { pg8::Gemm g{Yn, WSSD, M, D, D, SCY, WSC}; OrderTwice S; S.so.init(M, D, G, bx); S.R = (512 + G - 1) / G; EpiGate E{Gt, b_gate, MERGED};
;           pg8::gemm_phase<EpiGate, OrderTwice, true, true>(lds, g, S, E); }
.LBB0_880:
	s_cmp_lt_i32 s78, 7
	s_cselect_b64 s[0:1], -1, 0
	s_cmp_gt_i32 s79, 6
	s_cselect_b64 s[2:3], -1, 0
	s_and_b64 s[0:1], s[0:1], s[2:3]
	s_andn2_b64 vcc, exec, s[0:1]
	s_cbranch_vccnz .LBB0_993
	s_lshr_b32 s100, s88, 3
	s_and_b32 s100, s100, 31
	s_cmp_eq_u32 s100, 0
	s_cbranch_scc1 .Lskew6_done
.Lskew6_loop:
	s_sleep 3
	s_sub_u32 s100, s100, 1
	s_cmp_lg_u32 s100, 0
	s_cbranch_scc1 .Lskew6_loop
.Lskew6_done:
	s_abs_i32 s0, s86
	v_cvt_f32_u32_e32 v1, s0
	s_sub_i32 s5, 0, s0
	s_add_i32 s1, s86, 0x1ff
	s_xor_b32 s4, s1, s86
	v_rcp_iflag_f32_e32 v1, v1
	s_abs_i32 s1, s1
	s_ashr_i32 s4, s4, 31
	s_mov_b64 s[2:3], s[74:75]
	v_mul_f32_e32 v1, 0x4f7ffffe, v1
	v_cvt_u32_f32_e32 v1, v1
	v_mov_b64_e32 v[2:3], 0x200
	v_readfirstlane_b32 s12, v0
	v_readfirstlane_b32 s6, v1
	s_mul_i32 s5, s5, s6
	s_mul_hi_u32 s5, s6, s5
	s_add_i32 s6, s6, s5
	s_mul_hi_u32 s5, s1, s6
	s_mul_i32 s6, s5, s0
	s_sub_i32 s1, s1, s6
	s_add_i32 s7, s5, 1
	s_sub_i32 s6, s1, s0
	s_cmp_ge_u32 s1, s0
	s_cselect_b32 s5, s7, s5
	s_cselect_b32 s1, s6, s1
	s_add_i32 s6, s5, 1
	s_cmp_ge_u32 s1, s0
	s_cselect_b32 s0, s6, s5
	s_xor_b32 s0, s0, s4
	s_sub_i32 s6, s0, s4
	s_load_dwordx2 s[4:5], s[2:3], 0xd8
	s_load_dwordx2 s[0:1], s[2:3], 0x90
	s_min_i32 s2, s6, 0
	s_sub_i32 s2, 0, s2
	s_mul_i32 s3, s2, s87
	s_mul_hi_u32 s7, s2, s86
	s_add_i32 s7, s7, s3
	s_mul_i32 s2, s2, s86
	s_add_u32 s2, s2, s88
	s_addc_u32 s3, s7, s89
	v_cmp_lt_i64_e64 s[8:9], s[2:3], v[2:3]
	v_mov_b64_e32 v[2:3], 0x1ff
	v_cmp_gt_i64_e32 vcc, s[2:3], v[2:3]
	s_cbranch_vccnz .LBB0_887
	s_ashr_i32 s3, s2, 31
	s_lshr_b32 s3, s3, 29
	s_add_i32 s11, s2, s3
	s_and_b32 s3, s11, -8
	s_sub_i32 s7, s2, s3
	s_cmp_gt_i32 s7, -1
	s_cbranch_scc0 .LBB0_884
	s_lshl_b32 s10, s7, 6
	s_ashr_i32 s2, s11, 3
	s_cbranch_execz .LBB0_885
	s_branch .LBB0_886

;     __device__ __forceinline__ void init(int G_, int c_) { G = G_; c = c_; so.init(M, NPROJ, G_, c_); }
; #define PHASE_BASES() const KAS char* KA = (const KAS char*)__builtin_amdgcn_kernarg_segment_ptr(); asm volatile("" : "+s"(KA)); unsigned char* const ws = *(unsigned char* const KAS*)(KA + 8 * 27)
; __global__ void __launch_bounds__(NWAVES * 64, 2) mk_fwd(Args args) {
;     ...
;     if (IN(7)) { PHASE_BASES();
;         pg8::Gemm g{MERGED, WO, M, D, D}; pg8::StaticOrder S; S.init(M, D, G, bx); EpiBf16Plain E{OUTX, D};
;         pg8::gemm_phase<EpiBf16Plain, pg8::StaticOrder, true, true>(lds, g, S, E);
.LBB0_993:
	s_cmp_lt_i32 s78, 8
	s_waitcnt lgkmcnt(0)
	s_cselect_b64 s[0:1], -1, 0
	s_cmp_gt_i32 s79, 7
	s_cselect_b64 s[2:3], -1, 0
	s_and_b64 s[0:1], s[0:1], s[2:3]
	s_andn2_b64 vcc, exec, s[0:1]
	s_cbranch_vccnz .LBB0_1072
	s_lshr_b32 s100, s88, 3
	s_and_b32 s100, s100, 31
	s_cmp_eq_u32 s100, 0
	s_cbranch_scc1 .Lskew7_done

;     __device__ __forceinline__ void init(int G_, int c_) { G = G_; c = c_; so.init(M, NPROJ, G_, c_); }
;     __device__ __forceinline__ bool next(int i, pg8::Unit& u) const { const int s = i >= R ? 1 : 0; const bool ok = so.next(i - s * R, u); u.sel = s; return ok && i < 2 * R; }
;     __host__ __device__ __forceinline__ bool next(int i, Unit& u) const {
;         const long L = (long)i * G + c; if (L >= nwg) return false;
;         int wgid = (int)L; { const int q = nwg / NXCD, r = nwg % NXCD, xcd = wgid % NXCD, off = wgid / NXCD; wgid = (xcd < r ? xcd * (q + 1) : r * (q + 1) + (xcd - r) * q) + off; }
;         const int nig = WGM * nN, gid = wgid / nig, fm = gid * WGM, gsz = (nM - fm) < WGM ? (nM - fm) : WGM;
;         u.pm = fm + ((wgid % nig) % gsz); u.pn = (wgid % nig) / gsz; return true;
; __global__ void __launch_bounds__(NWAVES * 64, 2) mk_fwd(Args args) {
;     ...
;         pg8::Gemm g{MERGED, WO, M, D, D}; pg8::StaticOrder S; S.init(M, D, G, bx); EpiBf16Plain E{OUTX, D};
;         pg8::gemm_phase<EpiBf16Plain, pg8::StaticOrder, true, true>(lds, g, S, E);
.Lskew7_done:
	s_mov_b64 s[0:1], s[74:75]
	s_cmpk_gt_i32 s88, 0x1ff
	v_readfirstlane_b32 s9, v0
	s_cbranch_scc1 .LBB0_1018
	s_load_dwordx2 s[4:5], s[0:1], 0xd8
	s_lshr_b32 s0, s89, 29
	s_add_i32 s3, s88, s0
	s_and_b32 s0, s3, -8
	s_sub_i32 s6, s88, s0
	s_cmp_gt_i32 s6, -1
	s_cbranch_scc0 .LBB0_997
	s_lshl_b32 s2, s6, 6
	s_cbranch_execz .LBB0_998
	s_branch .LBB0_999

; #define LAS __attribute__((address_space(3)))
;     __device__ __forceinline__ void init(int G_, int c_) { G = G_; c = c_; so.init(M, NPROJ, G_, c_); }
; #define PHASE_BASES() const KAS char* KA = (const KAS char*)__builtin_amdgcn_kernarg_segment_ptr(); asm volatile("" : "+s"(KA)); unsigned char* const ws = *(unsigned char* const KAS*)(KA + 8 * 27)
; __global__ void __launch_bounds__(NWAVES * 64, 2) mk_fwd(Args args) {
;     ...
;     if (IN(10)) { PHASE_BASES();
;         pg8::Gemm g{HX2, W13, NB * NE * CAP, NE * 2 * FF, D}; OrderMoe<16> S; S.init(G, bx); EpiMoe1 E{ACT};
;         pg8::gemm_phase_gather<EpiMoe1, OrderMoe<16>>(lds, g, IDX, (LAS int*)(lds + 131072), S, E);
.LBB0_1258:
	s_cmp_lt_i32 s78, 11
	s_cselect_b64 s[0:1], -1, 0
	s_cmp_gt_i32 s79, 10
	s_cselect_b64 s[2:3], -1, 0
	s_and_b64 s[0:1], s[0:1], s[2:3]
	s_andn2_b64 vcc, exec, s[0:1]
	s_cbranch_vccnz .LBB0_1339
	s_lshr_b32 s100, s88, 3
	s_and_b32 s100, s100, 31
	s_cmp_eq_u32 s100, 0
	s_cbranch_scc1 .Lskew10_done

;     __device__ __forceinline__ void init(int G_, int c_) { G = G_; c = c_; so.init(M, NPROJ, G_, c_); }
; #define PHASE_BASES() const KAS char* KA = (const KAS char*)__builtin_amdgcn_kernarg_segment_ptr(); asm volatile("" : "+s"(KA)); unsigned char* const ws = *(unsigned char* const KAS*)(KA + 8 * 27)
; __global__ void __launch_bounds__(NWAVES * 64, 2) mk_fwd(Args args) {
;     ...
;     if (IN(11)) { PHASE_BASES();
;         pg8::Gemm g{ACT, W2, NB * NE * CAP, NE * D, FF}; OrderMoe<8> S; S.init(G, bx); EpiMoe2 E{OUTE, VAL};
;         pg8::gemm_phase<EpiMoe2, OrderMoe<8>, true, true>(lds, g, S, E);
.LBB0_1339:
	s_cmp_lt_i32 s78, 12
	s_cselect_b64 s[0:1], -1, 0
	s_cmp_gt_i32 s79, 11
	s_cselect_b64 s[2:3], -1, 0
	s_and_b64 s[0:1], s[0:1], s[2:3]
	s_andn2_b64 vcc, exec, s[0:1]
	s_cbranch_vccnz .LBB0_1410
	s_lshr_b32 s100, s88, 3
	s_and_b32 s100, s100, 31
	s_cmp_eq_u32 s100, 0
	s_cbranch_scc1 .Lskew11_done

; #define PG8_STAGE(bufoff, gbase, voff) do { _Pragma("unroll") for (int _i = 0; _i < 2; ++_i) \
;         __builtin_amdgcn_global_load_lds((const unsigned*)((const char*)(gbase) + (voff)[_i]), (PG8_LAS unsigned*)(lds + (bufoff) + ldsw + _i * 8192), 16, 0, 0); } while (0)
; #define PG8_BAR __builtin_amdgcn_s_barrier()
; #define PG8_BAR __builtin_amdgcn_s_barrier()
; template <class Epi, class Sched, bool ALIGN_EPI = false, bool SP2 = false>
; __device__ __forceinline__ void gemm_phase(PG8_LAS unsigned char* lds, const Gemm g, const Sched& S, const Epi& E) {
;     ...
;     for (int i = 0; i < 2; ++i) { int R, C; stage_rc(tid * 16 + i * 8192, R, C); const int Rb = Epi::PERM ? ((R & ~31) + perm32(R & 31)) : R;
;         voffA[i] = (unsigned)(R * K + C) * 2u; voffB[i] = (unsigned)(Rb * K + C) * 2u; }
;     const size_t kstep = (size_t)(BK * 2);
;     const size_t hstep = (size_t)HALF * K * 2;
;     const size_t tstep = 2 * hstep;
;     const unsigned ldsw = (unsigned)wid * 1024u;
;     const int aoff = lds_byte(wr * 64 + fr, fq * 8), boff = lds_byte(wc * 32 + fr, fq * 8);
;     ...
;     Unit cur, nxt; int ui = 0;
;     if (!S.next(0, cur)) return;
;     f32x4 acc[2][2][4][2];
; #pragma unroll
;     for (int a = 0; a < 2; ++a)
; #pragma unroll
;         for (int b = 0; b < 2; ++b)
; #pragma unroll
;             for (int m = 0; m < 4; ++m)
; #pragma unroll
;                 for (int n = 0; n < 2; ++n) acc[a][b][m][n] = (f32x4){0.f, 0.f, 0.f, 0.f};
;     bf16x8 At[4][2], B0[2][2], B1[2][2];
;     const char* cA = (const char*)(cur.sel ? g.A2 : g.A) + (size_t)cur.pm * tstep; const char* cB = (const char*)(cur.sel ? g.Bt2 : g.Bt) + (size_t)cur.pn * tstep;
;     S.a_ready(cur);
;     if constexpr (SP2) {
;         PG8_STAGE(PG8_SB(0, 0), cB, voffB); PG8_STAGE(PG8_SB(0, 1), cB + hstep, voffB); PG8_STAGE(PG8_SA(0, 0), cA, voffA); PG8_STAGE(PG8_SA(0, 1), cA + hstep, voffA);
;         if (wr == 1) PG8_BAR;
;     __device__ __forceinline__ bool next(int i, pg8::Unit& u) const {
;         constexpr int NWG = NE * 8 * NJ, Q = NWG / 8;
;         const int L = i * G + c; if (L >= NWG) return false;
;         const int wgid = (L % 8) * Q + L / 8;
;         const int e = wgid / (8 * NJ), w = wgid % (8 * NJ), rt = w % 8, j = w / 8, b = rt >> 1, half = rt & 1;
;         u.pm = (b * NE + e) * 2 + half; u.pn = e * NJ + j; return true;
.Lskew11_done:
	s_mov_b64 s[0:1], s[74:75]
	s_cmpk_gt_i32 s88, 0x3ff
	v_readfirstlane_b32 s10, v0
	s_cbranch_scc1 .LBB0_1356
	s_load_dwordx2 s[6:7], s[0:1], 0xd8
	v_lshrrev_b32_e32 v1, 5, v0
	v_lshrrev_b32_e32 v3, 1, v0
	v_and_b32_e32 v1, 4, v1
	v_bfe_u32 v2, v0, 2, 2
	v_and_b32_e32 v12, 24, v3
	v_lshlrev_b32_e32 v3, 4, v0
	s_waitcnt lgkmcnt(0)
	s_add_u32 s33, s6, 0x2800000
	v_or3_b32 v2, v1, v2, v12
	v_or_b32_e32 v1, 0x2000, v3
	s_addc_u32 s40, s7, 0
	v_lshrrev_b32_e32 v4, 7, v1
	s_movk_i32 s0, 0x60
	s_add_u32 s41, s6, 0x39700000
	v_and_or_b32 v5, v4, s0, v2
	v_bfe_u32 v13, v0, 2, 4
	s_movk_i32 s0, 0x70
	s_addc_u32 s42, s7, 0
	v_and_or_b32 v4, v4, s0, v13
	s_lshr_b32 s0, s89, 29
	s_add_i32 s0, s88, s0
	s_ashr_i32 s0, s0, 3
	s_lshl_b32 s1, s88, 7
	s_mulk_i32 s0, 0xfc01
	s_add_i32 s0, s0, s1
	s_ashr_i32 s1, s0, 31
	s_lshr_b32 s1, s1, 26
	s_add_i32 s1, s0, s1
	s_ashr_i32 s2, s1, 6
	s_andn2_b32 s1, s1, 63
	s_sub_i32 s0, s0, s1
	s_bfe_i32 s1, s0, 0x80000
	s_bfe_u32 s1, s1, 0x3000c
	s_add_i32 s1, s0, s1
	s_bfe_i32 s3, s1, 0x80000
	s_and_b32 s1, s1, 0xf8
	s_sub_i32 s0, s0, s1
	s_sext_i32_i16 s3, s3
	s_sext_i32_i8 s0, s0
	s_ashr_i32 s1, s3, 3
	s_and_b32 s3, s0, 1
	s_lshl_b32 s0, s0, 3
	s_and_b32 s0, s0, 0x7ffffff0
	s_add_i32 s0, s0, s2
	s_lshl_b32 s0, s0, 1
	s_or_b32 s30, s0, s3
	s_lshl_b32 s0, s2, 3
	v_and_b32_e32 v6, 32, v0
	s_add_i32 s28, s0, s1
	s_lshr_b32 s8, s10, 6
	v_bitop3_b32 v10, v3, v6, 48 bitop3:0x6c
	v_and_b32_e32 v11, 64, v0
	s_ashr_i32 s31, s30, 31
	s_ashr_i32 s29, s28, 31
	s_lshr_b32 s11, s10, 8
	s_lshl_b32 s43, s8, 10
	v_or_b32_e32 v3, v10, v11
	s_lshl_b64 s[0:1], s[30:31], 20
	s_lshl_b64 s[2:3], s[28:29], 20
	s_waitcnt vmcnt(0)
	v_lshl_or_b32 v130, v4, 12, v3
	v_lshrrev_b32_e32 v4, 3, v0
	s_add_u32 s36, s41, s2
	v_and_or_b32 v2, v4, 32, v2
	s_addc_u32 s37, s42, s3
	s_add_i32 s29, s43, 0
	v_lshl_or_b32 v132, v2, 12, v3
	s_add_i32 m0, s29, 0x10000
	v_lshl_or_b32 v128, v5, 12, v3
	global_load_lds_dwordx4 v132, s[36:37]
	s_add_i32 m0, s29, 0x12000
	s_add_u32 s2, s36, 0x80000
	global_load_lds_dwordx4 v128, s[36:37]
	s_addc_u32 s3, s37, 0
	s_add_i32 m0, s29, 0x14000
	v_and_or_b32 v2, v4, 48, v13
	global_load_lds_dwordx4 v132, s[2:3]
	s_add_i32 m0, s29, 0x16000
	s_add_u32 s34, s33, s0
	s_addc_u32 s35, s40, s1
	s_add_i32 s31, s29, 0x2000
	v_lshl_or_b32 v134, v2, 12, v3
	global_load_lds_dwordx4 v128, s[2:3]
	s_mov_b32 m0, s29
	s_add_u32 s0, s34, 0x80000
	global_load_lds_dwordx4 v134, s[34:35]
	s_mov_b32 m0, s31
	s_addc_u32 s1, s35, 0
	s_add_i32 s44, s29, 0x4000
	global_load_lds_dwordx4 v130, s[34:35]
	s_mov_b32 m0, s44
	s_add_i32 s45, s29, 0x6000
	global_load_lds_dwordx4 v134, s[0:1]
	s_mov_b32 m0, s45
	v_mov_b32_e32 v137, 0
	global_load_lds_dwordx4 v130, s[0:1]
	v_mov_b32_e32 v133, v137
	v_mov_b32_e32 v129, v137
	v_mov_b32_e32 v135, v137
	v_mov_b32_e32 v131, v137
	s_cmp_eq_u32 s11, 1
	s_mov_b32 s46, 0
	v_lshl_add_u64 v[8:9], s[36:37], 0, v[132:133]
	v_lshl_add_u64 v[4:5], s[36:37], 0, v[128:129]
	s_mov_b64 s[0:1], 0x80000
	v_lshl_add_u64 v[2:3], s[34:35], 0, v[134:135]
	s_cselect_b64 s[2:3], -1, 0
	s_cmp_lg_u32 s11, 1
	v_lshl_add_u64 v[6:7], s[34:35], 0, v[130:131]
	s_cbranch_scc1 .LBB0_1343
	s_barrier
